# P13/P15 per-token streaming loads (expert ids, h2 slice, coefficients) tagged nt; stores and X left default
# baseline (speedup 1.0000x reference)
; #define LDS_WAIT() asm volatile("s_waitcnt lgkmcnt(0)" ::: "memory")
; __device__ __forceinline__ void phase_peer_v(const Frame& F, const Args& a, const bool dry) {
;     ...
;         for (; tok < T; tok += nrank * 8) {
;             lpe[lane] = pn0; lpe[64 + lane] = pn1; if (lane < 32) lcq[lane] = cn;
;             LDS_WAIT();
;             { const int tn = tok + nrank * 8; if (tn < T) { pn0 = PE[(size_t)tn * 128 + lane]; pn1 = PE[(size_t)tn * 128 + 64 + lane]; cn = CQ[(size_t)tn * 32 + (lane & 31)]; } }
;             u32x2* xp = (u32x2*)(X + (size_t)tok * D + sl * 256 + li * 16 + rg * 4);
;             const u32x2 xb = *xp; const f32x4 xq = {bflo(xb.x), bfhi(xb.x), bflo(xb.y), bfhi(xb.y)};
;             const float csc = CSC[tok];
;             i32x4 acc = {0, 0, 0, 0};
; #pragma unroll
;             for (int q8 = 0; q8 < 32 / PS_B; ++q8) { u32x4 w[PS_B]; unsigned cd[PS_B];
; #pragma unroll
;                 for (int j = 0; j < PS_B; ++j) { const int q = q8 * PS_B + j; const int e = lpe[4 * q + rg]; cd[j] = lcq[q]; w[j] = *(const u32x4*)(Vs + (size_t)e * 256); }
.LBB0_1585:
	ds_read2_b32 v[10:11], v145 offset1:4
	global_load_dwordx2 v[140:141], v[138:139], off
	ds_read2_b32 v[12:13], v145 offset0:8 offset1:12
	ds_read_b128 v[86:89], v144 offset:512
	ds_read_b128 v[14:17], v144 offset:528
	ds_read_b128 v[6:9], v144 offset:544
	ds_read_b128 v[2:5], v144 offset:560
	s_waitcnt lgkmcnt(3)
	v_bfe_u32 v86, v86, v146, 8
	v_ashrrev_i32_e32 v19, 31, v10
	v_mov_b32_e32 v18, v10
	v_lshlrev_b64 v[18:19], 8, v[18:19]
	v_ashrrev_i32_e32 v21, 31, v11
	v_mov_b32_e32 v20, v11
	v_lshl_add_u64 v[18:19], v[136:137], 0, v[18:19]
	v_lshlrev_b64 v[10:11], 8, v[20:21]
	v_lshl_add_u64 v[10:11], v[136:137], 0, v[10:11]
	global_load_dwordx4 v[118:121], v[18:19], off
	global_load_dwordx4 v[106:109], v[10:11], off
	v_ashrrev_i32_e32 v11, 31, v12
	v_mov_b32_e32 v10, v12
	v_lshlrev_b64 v[10:11], 8, v[10:11]
	v_ashrrev_i32_e32 v19, 31, v13
	v_mov_b32_e32 v18, v13
	v_lshl_add_u64 v[10:11], v[136:137], 0, v[10:11]
	v_lshlrev_b64 v[18:19], 8, v[18:19]
	ds_read2_b32 v[12:13], v145 offset0:16 offset1:20
	v_lshl_add_u64 v[18:19], v[136:137], 0, v[18:19]
	global_load_dwordx4 v[114:117], v[10:11], off
	global_load_dwordx4 v[98:101], v[18:19], off
	v_lshlrev_b32_e32 v86, v1, v86
	v_cndmask_b32_e64 v150, 0, v86, s[12:13]
	s_waitcnt lgkmcnt(0)
	v_ashrrev_i32_e32 v11, 31, v12
	v_mov_b32_e32 v10, v12
	v_lshlrev_b64 v[10:11], 8, v[10:11]
	v_ashrrev_i32_e32 v19, 31, v13
	v_mov_b32_e32 v18, v13
	v_lshl_add_u64 v[10:11], v[136:137], 0, v[10:11]
	v_lshlrev_b64 v[18:19], 8, v[18:19]
	ds_read2_b32 v[12:13], v145 offset0:24 offset1:28
	v_lshl_add_u64 v[18:19], v[136:137], 0, v[18:19]
	global_load_dwordx4 v[110:113], v[10:11], off
	global_load_dwordx4 v[90:93], v[18:19], off
	v_cndmask_b32_e64 v151, 0, v86, s[14:15]
	v_bfe_u32 v14, v14, v146, 8
	s_waitcnt lgkmcnt(0)
	v_ashrrev_i32_e32 v11, 31, v12
	v_mov_b32_e32 v10, v12
	v_lshlrev_b64 v[10:11], 8, v[10:11]
	v_ashrrev_i32_e32 v19, 31, v13
	v_mov_b32_e32 v18, v13
	v_lshl_add_u64 v[10:11], v[136:137], 0, v[10:11]
	v_lshlrev_b64 v[18:19], 8, v[18:19]
	ds_read2_b32 v[12:13], v145 offset0:32 offset1:36
	v_lshl_add_u64 v[18:19], v[136:137], 0, v[18:19]
	global_load_dwordx4 v[102:105], v[10:11], off
	global_load_dwordx4 v[82:85], v[18:19], off
	v_lshlrev_b32_e32 v14, v1, v14
	v_bfe_u32 v6, v6, v146, 8
	s_waitcnt lgkmcnt(0)
	v_ashrrev_i32_e32 v11, 31, v12
	v_mov_b32_e32 v10, v12
	v_lshlrev_b64 v[10:11], 8, v[10:11]
	v_ashrrev_i32_e32 v19, 31, v13
	v_mov_b32_e32 v18, v13
	v_lshl_add_u64 v[10:11], v[136:137], 0, v[10:11]
	v_lshlrev_b64 v[18:19], 8, v[18:19]
	ds_read2_b32 v[12:13], v145 offset0:40 offset1:44
	v_lshl_add_u64 v[18:19], v[136:137], 0, v[18:19]
	global_load_dwordx4 v[94:97], v[10:11], off
	global_load_dwordx4 v[74:77], v[18:19], off
	v_lshlrev_b32_e32 v6, v1, v6
	v_bfe_u32 v2, v2, v146, 8
	s_waitcnt lgkmcnt(0)
	v_ashrrev_i32_e32 v11, 31, v12
	v_mov_b32_e32 v10, v12
	v_lshlrev_b64 v[10:11], 8, v[10:11]
	v_ashrrev_i32_e32 v19, 31, v13
	v_mov_b32_e32 v18, v13
	v_lshl_add_u64 v[10:11], v[136:137], 0, v[10:11]
	ds_read2_b32 v[12:13], v145 offset0:48 offset1:52
	v_lshlrev_b64 v[18:19], 8, v[18:19]
	v_lshl_add_u64 v[18:19], v[136:137], 0, v[18:19]
	global_load_dwordx4 v[78:81], v[10:11], off
	global_load_dwordx4 v[66:69], v[18:19], off
	v_lshlrev_b32_e32 v2, v1, v2
	s_waitcnt lgkmcnt(0)
	v_ashrrev_i32_e32 v11, 31, v12
	v_mov_b32_e32 v10, v12
	v_ashrrev_i32_e32 v19, 31, v13
	v_mov_b32_e32 v18, v13
	ds_read2_b32 v[12:13], v145 offset0:56 offset1:60
	v_lshlrev_b64 v[10:11], 8, v[10:11]
	v_lshlrev_b64 v[18:19], 8, v[18:19]
	v_lshl_add_u64 v[10:11], v[136:137], 0, v[10:11]
	v_lshl_add_u64 v[18:19], v[136:137], 0, v[18:19]
	global_load_dwordx4 v[70:73], v[10:11], off
	global_load_dwordx4 v[58:61], v[18:19], off
	s_waitcnt lgkmcnt(0)
	v_ashrrev_i32_e32 v11, 31, v12
	v_mov_b32_e32 v10, v12
	v_ashrrev_i32_e32 v19, 31, v13
	v_mov_b32_e32 v18, v13
	ds_read2_b32 v[12:13], v145 offset0:64 offset1:68
	v_lshlrev_b64 v[10:11], 8, v[10:11]
	v_lshl_add_u64 v[10:11], v[136:137], 0, v[10:11]
	v_lshlrev_b64 v[18:19], 8, v[18:19]
	v_lshl_add_u64 v[18:19], v[136:137], 0, v[18:19]
	global_load_dwordx4 v[62:65], v[10:11], off
	global_load_dwordx4 v[46:49], v[18:19], off
	s_waitcnt lgkmcnt(0)
	v_ashrrev_i32_e32 v11, 31, v12
	v_mov_b32_e32 v10, v12
	v_lshlrev_b64 v[10:11], 8, v[10:11]
	v_ashrrev_i32_e32 v19, 31, v13
	v_mov_b32_e32 v18, v13
	v_lshl_add_u64 v[10:11], v[136:137], 0, v[10:11]
	ds_read2_b32 v[12:13], v145 offset0:72 offset1:76
	v_lshlrev_b64 v[18:19], 8, v[18:19]
	v_lshl_add_u64 v[18:19], v[136:137], 0, v[18:19]
	global_load_dwordx4 v[50:53], v[10:11], off
	global_load_dwordx4 v[38:41], v[18:19], off
	ds_read2_b32 v[20:21], v145 offset0:80 offset1:84
	s_waitcnt lgkmcnt(1)
	v_ashrrev_i32_e32 v19, 31, v13
	v_mov_b32_e32 v18, v13
	v_ashrrev_i32_e32 v11, 31, v12
	v_mov_b32_e32 v10, v12
	v_lshlrev_b64 v[12:13], 8, v[18:19]
	s_waitcnt lgkmcnt(0)
	v_ashrrev_i32_e32 v19, 31, v20
	v_mov_b32_e32 v18, v20
	v_ashrrev_i32_e32 v23, 31, v21
	v_mov_b32_e32 v22, v21
	v_lshlrev_b64 v[10:11], 8, v[10:11]
	v_lshlrev_b64 v[18:19], 8, v[18:19]
	v_lshlrev_b64 v[22:23], 8, v[22:23]
	v_lshl_add_u64 v[10:11], v[136:137], 0, v[10:11]
	v_lshl_add_u64 v[12:13], v[136:137], 0, v[12:13]
	v_lshl_add_u64 v[18:19], v[136:137], 0, v[18:19]
	v_lshl_add_u64 v[22:23], v[136:137], 0, v[22:23]
	global_load_dwordx4 v[42:45], v[10:11], off
	global_load_dwordx4 v[30:33], v[12:13], off
	ds_read_b128 v[54:57], v144 offset:576
	ds_read_b128 v[10:13], v144 offset:592
	ds_read2_b32 v[20:21], v145 offset0:88 offset1:92
	global_load_dwordx4 v[34:37], v[18:19], off
	s_nop 0
	global_load_dwordx4 v[22:25], v[22:23], off
	ds_read2_b32 v[152:153], v145 offset0:96 offset1:100
	s_waitcnt lgkmcnt(2)
; __device__ __forceinline__ void phase_peer_v(const Frame& F, const Args& a, const bool dry) {
;     ...
;             for (int q8 = 0; q8 < 32 / PS_B; ++q8) { u32x4 w[PS_B]; unsigned cd[PS_B];
; #pragma unroll
;                 for (int j = 0; j < PS_B; ++j) { const int q = q8 * PS_B + j; const int e = lpe[4 * q + rg]; cd[j] = lcq[q]; w[j] = *(const u32x4*)(Vs + (size_t)e * 256); }
; #pragma unroll
;                 for (int j = 0; j < PS_B; ++j) { const unsigned cb = ((cd[j] >> (8 * rg)) & 255u) << bsh;
;                     const u32x4 av = {dsel == 0 ? cb : 0u, dsel == 1 ? cb : 0u, dsel == 2 ? cb : 0u, dsel == 3 ? cb : 0u};
;                     acc = __builtin_amdgcn_mfma_i32_16x16x64_i8(__builtin_bit_cast(i32x4, av), __builtin_bit_cast(i32x4, w[j]), acc, 0, 0, 0); } }
	v_bfe_u32 v10, v10, v146, 8
	s_waitcnt lgkmcnt(1)
	v_ashrrev_i32_e32 v19, 31, v20
	v_mov_b32_e32 v18, v20
	s_waitcnt lgkmcnt(0)
	v_ashrrev_i32_e32 v149, 31, v152
	v_mov_b32_e32 v148, v152
	v_lshlrev_b64 v[148:149], 8, v[148:149]
	v_lshl_add_u64 v[156:157], v[136:137], 0, v[148:149]
	v_cndmask_b32_e64 v148, 0, v86, s[8:9]
	v_cndmask_b32_e64 v149, 0, v86, s[10:11]
	v_bfe_u32 v86, v87, v146, 8
	v_lshlrev_b32_e32 v86, v1, v86
	s_waitcnt vmcnt(21)
	v_mfma_i32_16x16x64_i8 v[118:121], v[148:151], v[118:121], 0
	v_cndmask_b32_e64 v148, 0, v86, s[8:9]
	v_cndmask_b32_e64 v149, 0, v86, s[10:11]
	v_cndmask_b32_e64 v150, 0, v86, s[12:13]
	v_cndmask_b32_e64 v151, 0, v86, s[14:15]
	v_ashrrev_i32_e32 v155, 31, v153
	v_mov_b32_e32 v154, v153
	v_bfe_u32 v86, v88, v146, 8
	v_lshlrev_b64 v[152:153], 8, v[154:155]
	v_lshlrev_b32_e32 v86, v1, v86
	v_lshl_add_u64 v[158:159], v[136:137], 0, v[152:153]
	v_cndmask_b32_e64 v152, 0, v86, s[8:9]
	v_cndmask_b32_e64 v153, 0, v86, s[10:11]
	v_cndmask_b32_e64 v154, 0, v86, s[12:13]
	v_cndmask_b32_e64 v155, 0, v86, s[14:15]
	s_waitcnt vmcnt(20)
	v_mfma_i32_16x16x64_i8 v[148:151], v[148:151], v[106:109], v[118:121]
	v_bfe_u32 v86, v89, v146, 8
	v_ashrrev_i32_e32 v27, 31, v21
	v_mov_b32_e32 v26, v21
	v_lshlrev_b32_e32 v89, v1, v86
	v_lshlrev_b64 v[18:19], 8, v[18:19]
	v_lshlrev_b64 v[20:21], 8, v[26:27]
	v_cndmask_b32_e64 v86, 0, v89, s[8:9]
	v_cndmask_b32_e64 v87, 0, v89, s[10:11]
	v_cndmask_b32_e64 v88, 0, v89, s[12:13]
	v_cndmask_b32_e64 v89, 0, v89, s[14:15]
	v_lshl_add_u64 v[18:19], v[136:137], 0, v[18:19]
	v_lshl_add_u64 v[20:21], v[136:137], 0, v[20:21]
	s_waitcnt vmcnt(19)
	v_mfma_i32_16x16x64_i8 v[114:117], v[152:155], v[114:117], v[148:151]
	global_load_dwordx4 v[26:29], v[18:19], off
	s_nop 0
	global_load_dwordx4 v[18:21], v[20:21], off
	s_nop 0
	global_load_dwordx4 v[118:121], v[156:157], off
	global_load_dwordx4 v[106:109], v[158:159], off
	ds_read2_b32 v[156:157], v145 offset0:104 offset1:108
	v_cndmask_b32_e64 v148, 0, v14, s[8:9]
	v_cndmask_b32_e64 v149, 0, v14, s[10:11]
	v_cndmask_b32_e64 v150, 0, v14, s[12:13]
	v_cndmask_b32_e64 v151, 0, v14, s[14:15]
	s_waitcnt vmcnt(22)
	v_mfma_i32_16x16x64_i8 v[86:89], v[86:89], v[98:101], v[114:117]
	v_bfe_u32 v14, v15, v146, 8
	s_waitcnt lgkmcnt(0)
	v_ashrrev_i32_e32 v99, 31, v156
	v_mov_b32_e32 v98, v156
	v_lshlrev_b32_e32 v14, v1, v14
	v_lshlrev_b64 v[114:115], 8, v[98:99]
	v_cndmask_b32_e64 v98, 0, v14, s[8:9]
	v_cndmask_b32_e64 v99, 0, v14, s[10:11]
	v_cndmask_b32_e64 v100, 0, v14, s[12:13]
	v_cndmask_b32_e64 v101, 0, v14, s[14:15]
	s_waitcnt vmcnt(21)
	v_mfma_i32_16x16x64_i8 v[86:89], v[148:151], v[110:113], v[86:89]
	v_bfe_u32 v14, v16, v146, 8
	v_lshlrev_b32_e32 v14, v1, v14
	v_cndmask_b32_e64 v110, 0, v14, s[8:9]
	v_cndmask_b32_e64 v111, 0, v14, s[10:11]
	v_cndmask_b32_e64 v112, 0, v14, s[12:13]
	v_cndmask_b32_e64 v113, 0, v14, s[14:15]
	s_waitcnt vmcnt(20)
	v_mfma_i32_16x16x64_i8 v[86:89], v[98:101], v[90:93], v[86:89]
	v_bfe_u32 v14, v17, v146, 8
	v_lshlrev_b32_e32 v17, v1, v14
	v_cndmask_b32_e64 v14, 0, v17, s[8:9]
	v_cndmask_b32_e64 v15, 0, v17, s[10:11]
	v_cndmask_b32_e64 v16, 0, v17, s[12:13]
	v_cndmask_b32_e64 v17, 0, v17, s[14:15]
	s_waitcnt vmcnt(19)
	v_mfma_i32_16x16x64_i8 v[86:89], v[110:113], v[102:105], v[86:89]
	v_cndmask_b32_e64 v90, 0, v6, s[8:9]
	v_cndmask_b32_e64 v91, 0, v6, s[10:11]
	v_cndmask_b32_e64 v92, 0, v6, s[12:13]
	v_cndmask_b32_e64 v93, 0, v6, s[14:15]
	s_waitcnt vmcnt(18)
	v_mfma_i32_16x16x64_i8 v[14:17], v[14:17], v[82:85], v[86:89]
	v_ashrrev_i32_e32 v101, 31, v157
	v_mov_b32_e32 v100, v157
	v_bfe_u32 v6, v7, v146, 8
	v_lshlrev_b64 v[82:83], 8, v[100:101]
	v_lshlrev_b32_e32 v6, v1, v6
	v_lshl_add_u64 v[100:101], v[136:137], 0, v[82:83]
	v_cndmask_b32_e64 v82, 0, v6, s[8:9]
	v_cndmask_b32_e64 v83, 0, v6, s[10:11]
	v_cndmask_b32_e64 v84, 0, v6, s[12:13]
	v_cndmask_b32_e64 v85, 0, v6, s[14:15]
	s_waitcnt vmcnt(17)
	v_mfma_i32_16x16x64_i8 v[14:17], v[90:93], v[94:97], v[14:17]
	v_bfe_u32 v6, v8, v146, 8
	v_lshlrev_b32_e32 v6, v1, v6
	ds_read2_b32 v[102:103], v145 offset0:112 offset1:116
	s_waitcnt vmcnt(16)
	v_mfma_i32_16x16x64_i8 v[14:17], v[82:85], v[74:77], v[14:17]
	v_cndmask_b32_e64 v74, 0, v6, s[8:9]
	v_cndmask_b32_e64 v75, 0, v6, s[10:11]
	v_cndmask_b32_e64 v76, 0, v6, s[12:13]
	v_cndmask_b32_e64 v77, 0, v6, s[14:15]
	v_bfe_u32 v6, v9, v146, 8
	v_lshlrev_b32_e32 v9, v1, v6
	v_cndmask_b32_e64 v6, 0, v9, s[8:9]
	v_cndmask_b32_e64 v7, 0, v9, s[10:11]
	v_cndmask_b32_e64 v8, 0, v9, s[12:13]
	v_cndmask_b32_e64 v9, 0, v9, s[14:15]
	s_waitcnt vmcnt(15)
	v_mfma_i32_16x16x64_i8 v[14:17], v[74:77], v[78:81], v[14:17]
	v_lshl_add_u64 v[98:99], v[136:137], 0, v[114:115]
	global_load_dwordx4 v[86:89], v[98:99], off
	global_load_dwordx4 v[90:93], v[100:101], off
	ds_read_b128 v[74:77], v144 offset:608
	ds_read_b128 v[78:81], v144 offset:624
	s_waitcnt vmcnt(16)
	v_mfma_i32_16x16x64_i8 v[6:9], v[6:9], v[66:69], v[14:17]
	s_waitcnt lgkmcnt(2)
	v_ashrrev_i32_e32 v95, 31, v102
	v_mov_b32_e32 v94, v102
	v_lshlrev_b64 v[82:83], 8, v[94:95]
	v_cndmask_b32_e64 v14, 0, v2, s[8:9]
	v_cndmask_b32_e64 v15, 0, v2, s[10:11]
	v_cndmask_b32_e64 v16, 0, v2, s[12:13]
	v_cndmask_b32_e64 v17, 0, v2, s[14:15]
	v_bfe_u32 v2, v3, v146, 8
	v_lshlrev_b32_e32 v2, v1, v2
	v_cndmask_b32_e64 v66, 0, v2, s[8:9]
	v_cndmask_b32_e64 v67, 0, v2, s[10:11]
	v_cndmask_b32_e64 v68, 0, v2, s[12:13]
	v_cndmask_b32_e64 v69, 0, v2, s[14:15]
	s_waitcnt vmcnt(15)
	v_mfma_i32_16x16x64_i8 v[6:9], v[14:17], v[70:73], v[6:9]
	v_bfe_u32 v2, v4, v146, 8
	v_lshlrev_b32_e32 v2, v1, v2
	v_cndmask_b32_e64 v14, 0, v2, s[8:9]
	v_cndmask_b32_e64 v15, 0, v2, s[10:11]
	v_cndmask_b32_e64 v16, 0, v2, s[12:13]
	v_cndmask_b32_e64 v17, 0, v2, s[14:15]
	s_waitcnt vmcnt(14)
; #define LDS_WAIT() asm volatile("s_waitcnt lgkmcnt(0)" ::: "memory")
; __device__ __forceinline__ unsigned cvtpk(float lo, float hi) { unsigned r; asm volatile("v_cvt_pk_bf16_f32 %0, %1, %2" : "=v"(r) : "v"(lo), "v"(hi)); return r; }
; __device__ __forceinline__ void phase_peer_v(const Frame& F, const Args& a, const bool dry) {
;     ...
;             for (int q8 = 0; q8 < 32 / PS_B; ++q8) { u32x4 w[PS_B]; unsigned cd[PS_B];
; #pragma unroll
;                 for (int j = 0; j < PS_B; ++j) { const int q = q8 * PS_B + j; const int e = lpe[4 * q + rg]; cd[j] = lcq[q]; w[j] = *(const u32x4*)(Vs + (size_t)e * 256); }
; #pragma unroll
;                 for (int j = 0; j < PS_B; ++j) { const unsigned cb = ((cd[j] >> (8 * rg)) & 255u) << bsh;
;                     const u32x4 av = {dsel == 0 ? cb : 0u, dsel == 1 ? cb : 0u, dsel == 2 ? cb : 0u, dsel == 3 ? cb : 0u};
;                     acc = __builtin_amdgcn_mfma_i32_16x16x64_i8(__builtin_bit_cast(i32x4, av), __builtin_bit_cast(i32x4, w[j]), acc, 0, 0, 0); } }
;             if (!dry) { f32x4 x0 = xq; x0.x += (float)acc[0] * csc; x0.y += (float)acc[1] * csc; x0.z += (float)acc[2] * csc; x0.w += (float)acc[3] * csc; *xp = (u32x2){cvtpk(x0.x, x0.y), cvtpk(x0.z, x0.w)}; }
;             LDS_WAIT();
	v_mfma_i32_16x16x64_i8 v[6:9], v[66:69], v[58:61], v[6:9]
	v_bfe_u32 v2, v5, v146, 8
	v_lshlrev_b32_e32 v5, v1, v2
	v_cndmask_b32_e64 v2, 0, v5, s[8:9]
	v_cndmask_b32_e64 v3, 0, v5, s[10:11]
	v_cndmask_b32_e64 v4, 0, v5, s[12:13]
	v_cndmask_b32_e64 v5, 0, v5, s[14:15]
	s_waitcnt vmcnt(13)
	v_mfma_i32_16x16x64_i8 v[6:9], v[14:17], v[62:65], v[6:9]
	v_ashrrev_i32_e32 v73, 31, v103
	v_mov_b32_e32 v72, v103
	v_lshlrev_b64 v[14:15], 8, v[72:73]
	s_waitcnt vmcnt(12)
	v_mfma_i32_16x16x64_i8 v[2:5], v[2:5], v[46:49], v[6:9]
	v_lshl_add_u64 v[58:59], v[136:137], 0, v[14:15]
	v_bfe_u32 v14, v55, v146, 8
	v_lshlrev_b32_e32 v17, v1, v14
	v_bfe_u32 v6, v54, v146, 8
	v_lshlrev_b32_e32 v9, v1, v6
	v_cndmask_b32_e64 v6, 0, v9, s[8:9]
	v_cndmask_b32_e64 v7, 0, v9, s[10:11]
	v_cndmask_b32_e64 v8, 0, v9, s[12:13]
	v_cndmask_b32_e64 v9, 0, v9, s[14:15]
	v_cndmask_b32_e64 v14, 0, v17, s[8:9]
	v_cndmask_b32_e64 v15, 0, v17, s[10:11]
	v_cndmask_b32_e64 v16, 0, v17, s[12:13]
	v_cndmask_b32_e64 v17, 0, v17, s[14:15]
	s_waitcnt vmcnt(11)
	v_mfma_i32_16x16x64_i8 v[2:5], v[6:9], v[50:53], v[2:5]
	ds_read2_b32 v[60:61], v145 offset0:120 offset1:124
	v_lshl_add_u64 v[70:71], v[136:137], 0, v[82:83]
	global_load_dwordx4 v[6:9], v[70:71], off
	global_load_dwordx4 v[46:49], v[58:59], off
	s_waitcnt vmcnt(12)
	v_mfma_i32_16x16x64_i8 v[2:5], v[14:17], v[38:41], v[2:5]
	v_bfe_u32 v14, v56, v146, 8
	v_lshlrev_b32_e32 v17, v1, v14
	v_cndmask_b32_e64 v14, 0, v17, s[8:9]
	v_cndmask_b32_e64 v15, 0, v17, s[10:11]
	v_cndmask_b32_e64 v16, 0, v17, s[12:13]
	v_cndmask_b32_e64 v17, 0, v17, s[14:15]
	v_bfe_u32 v38, v57, v146, 8
	v_lshlrev_b32_e32 v41, v1, v38
	v_cndmask_b32_e64 v38, 0, v41, s[8:9]
	v_cndmask_b32_e64 v39, 0, v41, s[10:11]
	v_cndmask_b32_e64 v40, 0, v41, s[12:13]
	v_cndmask_b32_e64 v41, 0, v41, s[14:15]
	s_waitcnt vmcnt(11)
	v_mfma_i32_16x16x64_i8 v[2:5], v[14:17], v[42:45], v[2:5]
	s_waitcnt lgkmcnt(0)
	v_ashrrev_i32_e32 v51, 31, v60
	v_mov_b32_e32 v50, v60
	v_lshlrev_b64 v[14:15], 8, v[50:51]
	v_lshlrev_b32_e32 v10, v1, v10
	v_lshl_add_u64 v[42:43], v[136:137], 0, v[14:15]
	v_cndmask_b32_e64 v14, 0, v10, s[8:9]
	v_cndmask_b32_e64 v15, 0, v10, s[10:11]
	v_cndmask_b32_e64 v16, 0, v10, s[12:13]
	v_cndmask_b32_e64 v17, 0, v10, s[14:15]
	s_waitcnt vmcnt(10)
	v_mfma_i32_16x16x64_i8 v[2:5], v[38:41], v[30:33], v[2:5]
	v_bfe_u32 v10, v11, v146, 8
	v_lshlrev_b32_e32 v10, v1, v10
	v_cndmask_b32_e64 v30, 0, v10, s[8:9]
	v_cndmask_b32_e64 v31, 0, v10, s[10:11]
	v_cndmask_b32_e64 v32, 0, v10, s[12:13]
	v_cndmask_b32_e64 v33, 0, v10, s[14:15]
	s_waitcnt vmcnt(9)
	v_mfma_i32_16x16x64_i8 v[2:5], v[14:17], v[34:37], v[2:5]
	v_ashrrev_i32_e32 v11, 31, v61
	v_mov_b32_e32 v10, v61
	v_lshlrev_b64 v[34:35], 8, v[10:11]
	v_bfe_u32 v10, v12, v146, 8
	v_lshlrev_b32_e32 v10, v1, v10
	v_cndmask_b32_e64 v14, 0, v10, s[8:9]
	v_cndmask_b32_e64 v15, 0, v10, s[10:11]
	v_cndmask_b32_e64 v16, 0, v10, s[12:13]
	v_cndmask_b32_e64 v17, 0, v10, s[14:15]
	s_waitcnt vmcnt(8)
	v_mfma_i32_16x16x64_i8 v[2:5], v[30:33], v[22:25], v[2:5]
	v_lshl_add_u64 v[22:23], v[136:137], 0, v[34:35]
	v_bfe_u32 v10, v13, v146, 8
	v_lshlrev_b32_e32 v13, v1, v10
	s_waitcnt vmcnt(7)
	v_mfma_i32_16x16x64_i8 v[2:5], v[14:17], v[26:29], v[2:5]
	global_load_dwordx4 v[14:17], v[42:43], off
	s_nop 0
	global_load_dwordx4 v[22:25], v[22:23], off
	v_cndmask_b32_e64 v10, 0, v13, s[8:9]
	v_cndmask_b32_e64 v11, 0, v13, s[10:11]
	v_cndmask_b32_e64 v12, 0, v13, s[12:13]
	v_cndmask_b32_e64 v13, 0, v13, s[14:15]
	s_waitcnt vmcnt(8)
	s_nop 0
	v_mfma_i32_16x16x64_i8 v[2:5], v[10:13], v[18:21], v[2:5]
	global_load_dword v18, v123, s[28:29] nt
	v_bfe_u32 v10, v74, v146, 8
	v_lshlrev_b32_e32 v13, v1, v10
	v_cndmask_b32_e64 v10, 0, v13, s[8:9]
	v_cndmask_b32_e64 v11, 0, v13, s[10:11]
	v_cndmask_b32_e64 v12, 0, v13, s[12:13]
	v_cndmask_b32_e64 v13, 0, v13, s[14:15]
	v_lshlrev_b32_e32 v19, 16, v140
	s_add_u32 s28, s28, s22
	s_waitcnt vmcnt(8)
	v_mfma_i32_16x16x64_i8 v[2:5], v[10:13], v[118:121], v[2:5]
	v_bfe_u32 v10, v75, v146, 8
	v_lshlrev_b32_e32 v13, v1, v10
	v_cndmask_b32_e64 v10, 0, v13, s[8:9]
	v_cndmask_b32_e64 v11, 0, v13, s[10:11]
	v_cndmask_b32_e64 v12, 0, v13, s[12:13]
	v_cndmask_b32_e64 v13, 0, v13, s[14:15]
	s_addc_u32 s29, s29, s23
	s_andn2_b64 vcc, exec, s[34:35]
	s_waitcnt vmcnt(7)
	v_mfma_i32_16x16x64_i8 v[2:5], v[10:13], v[106:109], v[2:5]
	v_bfe_u32 v10, v76, v146, 8
	v_lshlrev_b32_e32 v13, v1, v10
	v_cndmask_b32_e64 v10, 0, v13, s[8:9]
	v_cndmask_b32_e64 v11, 0, v13, s[10:11]
	v_cndmask_b32_e64 v12, 0, v13, s[12:13]
	v_cndmask_b32_e64 v13, 0, v13, s[14:15]
	s_waitcnt vmcnt(6)
	s_nop 0
	v_mfma_i32_16x16x64_i8 v[2:5], v[10:13], v[86:89], v[2:5]
	v_bfe_u32 v10, v77, v146, 8
	v_lshlrev_b32_e32 v13, v1, v10
	v_cndmask_b32_e64 v10, 0, v13, s[8:9]
	v_cndmask_b32_e64 v11, 0, v13, s[10:11]
	v_cndmask_b32_e64 v12, 0, v13, s[12:13]
	v_cndmask_b32_e64 v13, 0, v13, s[14:15]
	s_waitcnt vmcnt(5)
	s_nop 0
	v_mfma_i32_16x16x64_i8 v[2:5], v[10:13], v[90:93], v[2:5]
	v_bfe_u32 v10, v78, v146, 8
	v_lshlrev_b32_e32 v13, v1, v10
	v_cndmask_b32_e64 v10, 0, v13, s[8:9]
	v_cndmask_b32_e64 v11, 0, v13, s[10:11]
	v_cndmask_b32_e64 v12, 0, v13, s[12:13]
	v_cndmask_b32_e64 v13, 0, v13, s[14:15]
	s_waitcnt vmcnt(4)
	s_nop 0
	v_mfma_i32_16x16x64_i8 v[2:5], v[10:13], v[6:9], v[2:5]
	v_bfe_u32 v6, v79, v146, 8
	v_lshlrev_b32_e32 v9, v1, v6
	v_cndmask_b32_e64 v6, 0, v9, s[8:9]
	v_cndmask_b32_e64 v7, 0, v9, s[10:11]
	v_cndmask_b32_e64 v8, 0, v9, s[12:13]
	v_cndmask_b32_e64 v9, 0, v9, s[14:15]
	v_bfe_u32 v10, v81, v146, 8
	v_lshlrev_b32_e32 v13, v1, v10
	s_waitcnt vmcnt(3)
	v_mfma_i32_16x16x64_i8 v[2:5], v[6:9], v[46:49], v[2:5]
	v_bfe_u32 v6, v80, v146, 8
	v_lshlrev_b32_e32 v9, v1, v6
	v_cndmask_b32_e64 v6, 0, v9, s[8:9]
	v_cndmask_b32_e64 v7, 0, v9, s[10:11]
	v_cndmask_b32_e64 v8, 0, v9, s[12:13]
	v_cndmask_b32_e64 v9, 0, v9, s[14:15]
	v_cndmask_b32_e64 v10, 0, v13, s[8:9]
	v_cndmask_b32_e64 v11, 0, v13, s[10:11]
	v_cndmask_b32_e64 v12, 0, v13, s[12:13]
	v_cndmask_b32_e64 v13, 0, v13, s[14:15]
	s_waitcnt vmcnt(2)
	v_mfma_i32_16x16x64_i8 v[2:5], v[6:9], v[14:17], v[2:5]
	v_and_b32_e32 v6, 0xffff0000, v140
	v_lshlrev_b32_e32 v7, 16, v141
	v_and_b32_e32 v8, 0xffff0000, v141
	s_waitcnt vmcnt(1)
	v_mfma_i32_16x16x64_i8 v[2:5], v[10:13], v[22:25], v[2:5]
	s_nop 7
	v_cvt_f32_i32_e32 v2, v2
	v_cvt_f32_i32_e32 v3, v3
	v_cvt_f32_i32_e32 v4, v4
	v_cvt_f32_i32_e32 v5, v5
	s_waitcnt vmcnt(0)
	v_fmac_f32_e32 v19, v18, v2
	v_fmac_f32_e32 v6, v18, v3
	v_fmac_f32_e32 v7, v18, v4
	v_fmac_f32_e32 v8, v18, v5
	v_cvt_pk_bf16_f32 v2, v19, v6
	v_cvt_pk_bf16_f32 v3, v7, v8
	global_store_dwordx2 v[138:139], v[2:3], off
	s_waitcnt lgkmcnt(0)
	v_lshl_add_u64 v[138:139], v[138:139], 0, s[24:25]
	s_cbranch_vccz .LBB0_1582
